# MLA fast path: role-split barriers (waves 0-3 sync after softmax phases, waves 4-7 after MFMA phases), two barriers per interval, no stagger barriers
# speedup vs baseline: 1.0041x; 1.0041x over previous
.Linit_done:
	s_waitcnt lgkmcnt(0)
	s_barrier
	v_mfma_f32_32x32x16_bf16 v[16:31], v[90:93], v[144:147], v[16:31]
	v_lshlrev_b32_e32 v145, 2, v204
	s_waitcnt vmcnt(5)
	v_pk_mul_f32 v[48:49], v[48:49], v[56:57] op_sel:[0,1] op_sel_hi:[0,0]
	v_pk_fma_f32 v[50:51], v[44:45], v[56:57], v[48:49] neg_lo:[0,0,1] neg_hi:[0,0,1]
	v_pk_fma_f32 v[44:45], v[44:45], v[56:57], v[48:49] op_sel_hi:[0,1,1]
	v_mul_f32_e32 v44, v168, v46
	v_mul_f32_e32 v46, v168, v47
	v_pk_mul_f32 v[46:47], v[46:47], v[58:59] op_sel:[0,1] op_sel_hi:[0,0]
	v_mfma_f32_32x32x16_bf16 v[16:31], v[82:85], v[140:143], v[16:31]
	v_fma_f32 v48, v44, v58, -v46
	v_fma_f32 v49, v45, v59, -v47
	v_fma_f32 v46, v44, v58, v46
	v_fma_f32 v47, v44, v59, v47
	v_mul_f32_e32 v44, v168, v41
	s_waitcnt vmcnt(4)
	v_pk_mul_f32 v[52:53], v[44:45], v[60:61] op_sel:[0,1] op_sel_hi:[0,0]
	v_pk_fma_f32 v[54:55], v[40:41], v[60:61], v[52:53] neg_lo:[0,0,1] neg_hi:[0,0,1]
	v_pk_fma_f32 v[40:41], v[40:41], v[60:61], v[52:53] op_sel_hi:[0,1,1]
	v_mul_f32_e32 v40, v168, v42
	v_mfma_f32_32x32x16_bf16 v[16:31], v[160:163], v[132:135], v[16:31]
	v_mul_f32_e32 v42, v168, v43
	v_pk_mul_f32 v[42:43], v[42:43], v[62:63] op_sel:[0,1] op_sel_hi:[0,0]
	v_pk_fma_f32 v[52:53], v[40:41], v[62:63], v[42:43] neg_lo:[0,0,1] neg_hi:[0,0,1]
	v_pk_fma_f32 v[42:43], v[40:41], v[62:63], v[42:43] op_sel_hi:[0,1,1]
	v_cvt_pk_bf16_f32 v132, v54, v41
	v_cvt_pk_bf16_f32 v133, v52, v43
	v_cvt_pk_bf16_f32 v134, v50, v45
	v_mfma_f32_32x32x16_bf16 v[16:31], v[176:179], v[136:139], v[16:31]
	v_cvt_pk_bf16_f32 v135, v48, v47
	v_mov_b64_e32 v[62:63], v[14:15]
	v_mov_b64_e32 v[60:61], v[12:13]
	v_mov_b64_e32 v[58:59], v[10:11]
	v_mov_b64_e32 v[56:57], v[8:9]
	v_mov_b64_e32 v[54:55], v[6:7]
	v_mov_b64_e32 v[52:53], v[4:5]
	s_nop 4
	v_mul_f32_e32 v40, v168, v21
	v_mul_f32_e32 v20, v168, v20
	s_waitcnt vmcnt(2)
	v_pk_mul_f32 v[40:41], v[40:41], v[64:65] op_sel:[0,1] op_sel_hi:[0,0]
	v_pk_fma_f32 v[42:43], v[20:21], v[64:65], v[40:41] neg_lo:[0,0,1] neg_hi:[0,0,1]
	v_pk_fma_f32 v[20:21], v[20:21], v[64:65], v[40:41] op_sel_hi:[0,1,1]
	v_mul_f32_e32 v20, v168, v22
	v_mul_f32_e32 v22, v168, v23
	v_pk_mul_f32 v[22:23], v[22:23], v[66:67] op_sel:[0,1] op_sel_hi:[0,0]
	v_pk_fma_f32 v[40:41], v[20:21], v[66:67], v[22:23] neg_lo:[0,0,1] neg_hi:[0,0,1]
	v_pk_fma_f32 v[22:23], v[20:21], v[66:67], v[22:23] op_sel_hi:[0,1,1]
	v_mul_f32_e32 v20, v168, v17
	v_mul_f32_e32 v16, v168, v16
	v_pk_mul_f32 v[44:45], v[20:21], v[164:165] op_sel:[0,1] op_sel_hi:[0,0]
	v_pk_fma_f32 v[46:47], v[16:17], v[164:165], v[44:45] neg_lo:[0,0,1] neg_hi:[0,0,1]
	v_pk_fma_f32 v[16:17], v[16:17], v[164:165], v[44:45] op_sel_hi:[0,1,1]
	v_mul_f32_e32 v16, v168, v18
	v_mul_f32_e32 v18, v168, v19
	v_pk_mul_f32 v[18:19], v[18:19], v[166:167] op_sel:[0,1] op_sel_hi:[0,0]
	v_pk_fma_f32 v[44:45], v[16:17], v[166:167], v[18:19] neg_lo:[0,0,1] neg_hi:[0,0,1]
	v_pk_fma_f32 v[18:19], v[16:17], v[166:167], v[18:19] op_sel_hi:[0,1,1]
	v_mul_f32_e32 v18, v168, v29
	v_cvt_pk_bf16_f32 v137, v44, v19
	v_mul_f32_e32 v16, v168, v28
	s_waitcnt vmcnt(1)
	v_pk_mul_f32 v[18:19], v[18:19], v[36:37] op_sel:[0,1] op_sel_hi:[0,0]
	v_cvt_pk_bf16_f32 v136, v46, v17
	v_cvt_pk_bf16_f32 v138, v42, v21
	v_pk_fma_f32 v[20:21], v[16:17], v[36:37], v[18:19] neg_lo:[0,0,1] neg_hi:[0,0,1]
	v_pk_fma_f32 v[16:17], v[16:17], v[36:37], v[18:19] op_sel_hi:[0,1,1]
	v_mul_f32_e32 v18, v168, v31
	v_mul_f32_e32 v16, v168, v30
	v_pk_mul_f32 v[18:19], v[18:19], v[38:39] op_sel:[0,1] op_sel_hi:[0,0]
	v_cvt_pk_bf16_f32 v139, v40, v23
	v_pk_fma_f32 v[22:23], v[16:17], v[38:39], v[18:19] neg_lo:[0,0,1] neg_hi:[0,0,1]
	v_pk_fma_f32 v[18:19], v[16:17], v[38:39], v[18:19] op_sel_hi:[0,1,1]
	v_mul_f32_e32 v18, v168, v25
	v_mul_f32_e32 v16, v168, v24
	s_waitcnt vmcnt(0)
	v_pk_mul_f32 v[24:25], v[18:19], v[32:33] op_sel:[0,1] op_sel_hi:[0,0]
	v_mul_f32_e32 v18, v168, v27
	v_pk_fma_f32 v[28:29], v[16:17], v[32:33], v[24:25] neg_lo:[0,0,1] neg_hi:[0,0,1]
	v_pk_fma_f32 v[24:25], v[16:17], v[32:33], v[24:25] op_sel_hi:[0,1,1]
	v_mul_f32_e32 v16, v168, v26
	v_pk_mul_f32 v[26:27], v[18:19], v[34:35] op_sel:[0,1] op_sel_hi:[0,0]
	v_pk_fma_f32 v[30:31], v[16:17], v[34:35], v[26:27] neg_lo:[0,0,1] neg_hi:[0,0,1]
	v_pk_fma_f32 v[26:27], v[16:17], v[34:35], v[26:27] op_sel_hi:[0,1,1]
	v_cvt_pk_bf16_f32 v142, v20, v17
	v_lshrrev_b32_e32 v17, 1, v203
	v_mad_u32_u24 v16, v200, s4, 0
	v_bfe_u32 v18, v203, 1, 3
	v_bitop3_b32 v17, v204, v17, 7 bitop3:0x78
	v_lshl_add_u32 v147, v17, 4, v16
	v_bitop3_b32 v17, v204, v18, 2 bitop3:0x36
	v_lshl_add_u32 v148, v17, 4, v16
	v_bitop3_b32 v17, v204, v18, 4 bitop3:0x36
	v_lshl_add_u32 v149, v17, 4, v16
	v_bitop3_b32 v17, v204, v18, 6 bitop3:0x36
	v_lshl_add_u32 v150, v17, 4, v16
	v_lshrrev_b32_e32 v16, 3, v202
	v_bfe_u32 v17, v202, 3, 1
	v_and_b32_e32 v16, 2, v16
	v_bfe_u32 v18, v203, 1, 1
	v_bfe_u32 v20, v203, 2, 1
	v_lshlrev_b32_e32 v21, 3, v17
	v_cvt_pk_bf16_f32 v143, v22, v19
	v_or_b32_e32 v19, v16, v18
	v_or3_b32 v20, v21, v20, v145
	v_lshlrev_b32_e32 v21, 1, v204
	v_bitop3_b32 v16, v16, v21, v18 bitop3:0x36
	v_bitop3_b32 v18, v21, v19, 1 bitop3:0x36
	v_cvt_f32_ubyte0_e32 v21, s25
	v_lshlrev_b32_e32 v22, 3, v203
	v_lshlrev_b32_e32 v17, 6, v17
	v_lshlrev_b32_e32 v18, 4, v18
	v_rcp_iflag_f32_e32 v21, v21
	v_and_b32_e32 v22, 8, v22
	v_mad_u32_u24 v20, v20, s4, 0
	v_or_b32_e32 v19, v18, v17
	v_lshl_add_u32 v16, v16, 4, v20
	v_add3_u32 v152, v20, v19, v22
	v_xor_b32_e32 v19, 64, v17
	v_add3_u32 v151, v16, v17, v22
	v_add3_u32 v153, v16, v19, v22
	v_bitop3_b32 v16, v18, v17, 64 bitop3:0xf6
	v_add3_u32 v154, v20, v16, v22
	v_mul_f32_e32 v16, 0x4f7ffffe, v21
	v_cvt_u32_f32_e32 v16, v16
	s_abs_i32 s4, s89
	v_cvt_pk_bf16_f32 v140, v28, v25
	v_cvt_pk_bf16_f32 v141, v30, v27
	v_readfirstlane_b32 s6, v16
	s_mul_i32 s5, s5, s6
	s_mul_hi_u32 s5, s6, s5
	s_add_i32 s6, s6, s5
	s_mul_hi_u32 s5, s4, s6
	s_mul_i32 s6, s5, s25
	s_sub_i32 s4, s4, s6
	s_add_i32 s6, s5, 1
	s_sub_i32 s7, s4, s25
	s_cmp_ge_u32 s4, s25
	s_cselect_b32 s5, s6, s5
	s_cselect_b32 s4, s7, s4
	s_add_i32 s6, s5, 1
	s_cmp_ge_u32 s4, s25
	s_cselect_b32 s4, s6, s5
	s_xor_b32 s12, s4, s11
	s_sub_i32 s8, s12, s11
	s_mul_i32 s4, s8, s25
	s_sub_i32 s4, s89, s4
	s_lshl_b32 s6, s4, 5
	s_ashr_i32 s7, s6, 31
	s_lshl_b64 s[4:5], s[6:7], 2
	s_add_u32 s4, s68, s4
	s_addc_u32 s5, s69, s5
	v_lshl_or_b32 v16, s12, 6, v196
	s_lshl_b32 s7, s11, 6
	v_subrev_u32_e32 v155, s7, v16
	s_add_i32 s7, s29, s21
	v_add_u32_e32 v16, s7, v200
	v_sub_u32_e32 v156, v16, v145
	v_mov_b64_e32 v[46:47], v[14:15]
	v_mov_b64_e32 v[30:31], v[14:15]
	s_movk_i32 s7, 0x7f
	s_mov_b32 s11, 3
	s_mov_b32 s12, s40
	v_mov_b64_e32 v[44:45], v[12:13]
	v_mov_b64_e32 v[42:43], v[10:11]
	v_mov_b64_e32 v[40:41], v[8:9]
	v_mov_b64_e32 v[38:39], v[6:7]
	v_mov_b64_e32 v[36:37], v[4:5]
	v_mov_b64_e32 v[34:35], v[2:3]
	v_mov_b64_e32 v[32:33], v[0:1]
	v_mov_b64_e32 v[50:51], v[2:3]
	v_mov_b64_e32 v[48:49], v[0:1]
	v_mov_b64_e32 v[28:29], v[12:13]
	v_mov_b64_e32 v[26:27], v[10:11]
	v_mov_b64_e32 v[24:25], v[8:9]
	v_mov_b64_e32 v[22:23], v[6:7]
	v_mov_b64_e32 v[20:21], v[4:5]
	v_mov_b64_e32 v[18:19], v[2:3]
	v_mov_b64_e32 v[16:17], v[0:1]
.Lnostag_in:
	s_branch .LBB0_1238

.Lp1_nowait:
	s_cmp_eq_u32 s101, 0
	s_cbranch_scc1 .Lp1_bar
	s_cmp_lt_u32 s88, 0x1000
	s_cbranch_scc1 .Lp1_nobar

.Lp1_nobar:
	s_sub_i32 s15, s7, 64
	s_cmp_le_u32 s15, s44
	s_cbranch_scc1 .LBB0_1244
	v_add_u32_e32 v144, 123, v156
	v_cmp_le_i32_e64 s[16:17], 0, v144
	v_cmp_le_i32_e64 s[18:19], 32, v144
	v_cmp_le_i32_e64 vcc, 1, v144
	s_nop 4
	v_cndmask_b32_e64 v80, v199, v80, s[16:17]
	v_cmp_le_i32_e64 s[16:17], 33, v144
	v_cndmask_b32_e64 v64, v199, v64, s[18:19]
	v_cmp_le_i32_e64 s[18:19], 2, v144
	v_cndmask_b32_e64 v81, v199, v81, vcc
	v_cmp_le_i32_e64 vcc, 34, v144
	v_cndmask_b32_e64 v65, v199, v65, s[16:17]
	v_cmp_le_i32_e64 s[16:17], 3, v144
	v_cndmask_b32_e64 v82, v199, v82, s[18:19]
	v_cmp_le_i32_e64 s[18:19], 35, v144
	v_cndmask_b32_e64 v66, v199, v66, vcc
	v_cmp_le_i32_e64 vcc, 8, v144
	v_cndmask_b32_e64 v83, v199, v83, s[16:17]
	v_cmp_le_i32_e64 s[16:17], 40, v144
	v_cndmask_b32_e64 v67, v199, v67, s[18:19]
	v_cmp_le_i32_e64 s[18:19], 9, v144
	v_cndmask_b32_e64 v84, v199, v84, vcc
	v_cmp_le_i32_e64 vcc, 41, v144
	v_cndmask_b32_e64 v68, v199, v68, s[16:17]
	v_cmp_le_i32_e64 s[16:17], 10, v144
	v_cndmask_b32_e64 v85, v199, v85, s[18:19]
	v_cmp_le_i32_e64 s[18:19], 42, v144
	v_cndmask_b32_e64 v69, v199, v69, vcc
	v_cmp_le_i32_e64 vcc, 11, v144
	v_cndmask_b32_e64 v86, v199, v86, s[16:17]
	v_cmp_le_i32_e64 s[16:17], 43, v144
	v_cndmask_b32_e64 v70, v199, v70, s[18:19]
	v_cmp_le_i32_e64 s[18:19], 16, v144
	v_cndmask_b32_e64 v87, v199, v87, vcc
	v_cmp_le_i32_e64 vcc, 48, v144
	v_cndmask_b32_e64 v71, v199, v71, s[16:17]
	v_cmp_le_i32_e64 s[16:17], 17, v144
	v_cndmask_b32_e64 v88, v199, v88, s[18:19]
	v_cmp_le_i32_e64 s[18:19], 49, v144
	v_cndmask_b32_e64 v72, v199, v72, vcc
	v_cmp_le_i32_e64 vcc, 18, v144
	v_cndmask_b32_e64 v89, v199, v89, s[16:17]
	v_cmp_le_i32_e64 s[16:17], 50, v144
	v_cndmask_b32_e64 v73, v199, v73, s[18:19]
	v_cmp_le_i32_e64 s[18:19], 19, v144
	v_cndmask_b32_e64 v90, v199, v90, vcc
	v_cmp_le_i32_e64 vcc, 51, v144
	v_cndmask_b32_e64 v74, v199, v74, s[16:17]
	v_cmp_le_i32_e64 s[16:17], 24, v144
	v_cndmask_b32_e64 v91, v199, v91, s[18:19]
	v_cmp_le_i32_e64 s[18:19], 56, v144
	v_cndmask_b32_e64 v75, v199, v75, vcc
	v_cmp_le_i32_e64 vcc, 25, v144
	v_cndmask_b32_e64 v92, v199, v92, s[16:17]
	v_cmp_le_i32_e64 s[16:17], 57, v144
	v_cndmask_b32_e64 v76, v199, v76, s[18:19]
	v_cmp_le_i32_e64 s[18:19], 26, v144
	v_cndmask_b32_e64 v93, v199, v93, vcc
	v_cmp_le_i32_e64 vcc, 58, v144
	v_cndmask_b32_e64 v77, v199, v77, s[16:17]
	v_cmp_le_i32_e64 s[16:17], 27, v144
	v_cndmask_b32_e64 v94, v199, v94, s[18:19]
	v_cmp_le_i32_e64 s[18:19], 59, v144
	v_cndmask_b32_e64 v78, v199, v78, vcc
	v_cndmask_b32_e64 v95, v199, v95, s[16:17]
	v_cndmask_b32_e64 v79, v199, v79, s[18:19]

.Lno_bload:
	v_add_u32_e32 v248, s14, v151
	v_add_u32_e32 v249, s14, v152
	ds_read_b64_tr_b16 v[224:225], v248
	ds_read_b64_tr_b16 v[226:227], v249 offset:768
	ds_read_b64_tr_b16 v[228:229], v248 offset:128
	ds_read_b64_tr_b16 v[230:231], v249 offset:896
	ds_read_b64_tr_b16 v[232:233], v248 offset:6144
	ds_read_b64_tr_b16 v[234:235], v249 offset:6912
	ds_read_b64_tr_b16 v[236:237], v248 offset:6272
	ds_read_b64_tr_b16 v[238:239], v249 offset:7040
	ds_read_b64_tr_b16 v[240:241], v248 offset:12288
	ds_read_b64_tr_b16 v[242:243], v249 offset:13056
	ds_read_b64_tr_b16 v[244:245], v248 offset:12416
	ds_read_b64_tr_b16 v[246:247], v249 offset:13184
	ds_read_b64_tr_b16 v[252:253], v248 offset:18432
	ds_read_b64_tr_b16 v[254:255], v249 offset:19200
	ds_read_b64_tr_b16 v[204:205], v248 offset:18560
	ds_read_b64_tr_b16 v[206:207], v249 offset:19328
	v_exp_f32_e32 v80, v80
	v_exp_f32_e32 v81, v81
	v_exp_f32_e32 v82, v82
	v_exp_f32_e32 v83, v83
	v_add_f32_e32 v146, 0, v80
	v_exp_f32_e32 v84, v84
	v_add_f32_e32 v146, v81, v146
	v_exp_f32_e32 v85, v85
	v_add_f32_e32 v146, v82, v146
	v_exp_f32_e32 v86, v86
	v_add_f32_e32 v146, v83, v146
	v_exp_f32_e32 v87, v87
	v_add_f32_e32 v146, v84, v146
	v_exp_f32_e32 v88, v88
	v_add_f32_e32 v146, v85, v146
	v_exp_f32_e32 v89, v89
	v_add_f32_e32 v146, v86, v146
	v_exp_f32_e32 v90, v90
	v_add_f32_e32 v146, v87, v146
	v_exp_f32_e32 v91, v91
	v_add_f32_e32 v146, v88, v146
	v_exp_f32_e32 v92, v92
	v_add_f32_e32 v146, v89, v146
	v_exp_f32_e32 v93, v93
	v_add_f32_e32 v146, v90, v146
	v_exp_f32_e32 v94, v94
	v_add_f32_e32 v146, v91, v146
	v_exp_f32_e32 v95, v95
	v_add_f32_e32 v146, v92, v146
	v_exp_f32_e32 v64, v64
	v_add_f32_e32 v146, v93, v146
	v_exp_f32_e32 v65, v65
	v_add_f32_e32 v146, v94, v146
	v_exp_f32_e32 v66, v66
	v_add_f32_e32 v146, v95, v146
	v_exp_f32_e32 v67, v67
	v_add_f32_e32 v146, v64, v146
	v_exp_f32_e32 v68, v68
	v_add_f32_e32 v146, v65, v146
	v_exp_f32_e32 v69, v69
	v_add_f32_e32 v146, v66, v146
	v_exp_f32_e32 v70, v70
	v_add_f32_e32 v146, v67, v146
	v_exp_f32_e32 v71, v71
	v_add_f32_e32 v146, v68, v146
	v_exp_f32_e32 v161, v72
	v_add_f32_e32 v146, v69, v146
	v_add_f32_e32 v146, v70, v146
	v_add_f32_e32 v146, v71, v146
	v_add_f32_e32 v72, v161, v146
	v_exp_f32_e32 v146, v73
	v_exp_f32_e32 v162, v74
	v_exp_f32_e32 v163, v75
	v_exp_f32_e32 v164, v76
	v_add_f32_e32 v72, v146, v72
	v_exp_f32_e32 v165, v77
	v_add_f32_e32 v72, v162, v72
	v_exp_f32_e32 v166, v78
	v_add_f32_e32 v72, v163, v72
	v_exp_f32_e32 v167, v79
	v_add_f32_e32 v72, v164, v72
	v_add_f32_e32 v72, v165, v72
	v_add_f32_e32 v72, v166, v72
	v_cvt_pk_bf16_f32 v76, v80, v81
	v_cvt_pk_bf16_f32 v77, v84, v85
	v_cvt_pk_bf16_f32 v78, v82, v83
	v_cvt_pk_bf16_f32 v79, v86, v87
	v_cvt_pk_bf16_f32 v64, v64, v65
	v_cvt_pk_bf16_f32 v65, v68, v69
	v_cvt_pk_bf16_f32 v68, v161, v146
	v_add_f32_e32 v159, v167, v72
	v_cvt_pk_bf16_f32 v72, v88, v89
	v_cvt_pk_bf16_f32 v73, v92, v93
	v_cvt_pk_bf16_f32 v74, v90, v91
	v_cvt_pk_bf16_f32 v75, v94, v95
	v_cvt_pk_bf16_f32 v66, v66, v67
	v_cvt_pk_bf16_f32 v67, v70, v71
	v_cvt_pk_bf16_f32 v71, v166, v167
	v_cvt_pk_bf16_f32 v69, v164, v165
	v_cvt_pk_bf16_f32 v70, v162, v163
	v_add_u32_e32 v166, s14, v153
	v_add_u32_e32 v167, s14, v154
	s_cmp_ge_u32 s88, 0x1000
	s_cbranch_scc1 .Lb2
	s_barrier
.Lb2:
	s_add_i32 s14, s10, -2
	s_and_b32 s14, s14, 3
	s_mulk_i32 s14, 0x6000
	v_add_u32_e32 v146, s14, v147
	v_add_u32_e32 v161, s14, v148
	v_add_u32_e32 v144, s14, v149
	v_add_u32_e32 v168, s14, v150
	s_waitcnt lgkmcnt(14)
	v_mfma_f32_32x32x16_bf16 v[48:63], v[224:227], v[76:79], v[48:63]
	ds_read_b64_tr_b16 v[224:225], v166
	ds_read_b64_tr_b16 v[226:227], v167 offset:768
	s_waitcnt lgkmcnt(14)
	v_mfma_f32_32x32x16_bf16 v[0:15], v[228:231], v[76:79], v[0:15]
	ds_read_b64_tr_b16 v[228:229], v166 offset:128
	ds_read_b64_tr_b16 v[230:231], v167 offset:896
	s_waitcnt lgkmcnt(14)
	v_mfma_f32_32x32x16_bf16 v[48:63], v[232:235], v[72:75], v[48:63]
	ds_read_b64_tr_b16 v[232:233], v166 offset:6144
	ds_read_b64_tr_b16 v[234:235], v167 offset:6912
	s_waitcnt lgkmcnt(14)
	v_mfma_f32_32x32x16_bf16 v[0:15], v[236:239], v[72:75], v[0:15]
	ds_read_b64_tr_b16 v[236:237], v166 offset:6272
	ds_read_b64_tr_b16 v[238:239], v167 offset:7040
	s_waitcnt lgkmcnt(14)
	v_mfma_f32_32x32x16_bf16 v[48:63], v[240:243], v[64:67], v[48:63]
	ds_read_b64_tr_b16 v[240:241], v166 offset:12288
	ds_read_b64_tr_b16 v[242:243], v167 offset:13056
	s_waitcnt lgkmcnt(14)
	v_mfma_f32_32x32x16_bf16 v[0:15], v[244:247], v[64:67], v[0:15]
	ds_read_b64_tr_b16 v[244:245], v166 offset:12416
	ds_read_b64_tr_b16 v[246:247], v167 offset:13184
	s_waitcnt lgkmcnt(14)
	v_mfma_f32_32x32x16_bf16 v[48:63], v[252:255], v[68:71], v[48:63]
	ds_read_b64_tr_b16 v[252:253], v166 offset:18432
	ds_read_b64_tr_b16 v[254:255], v167 offset:19200
	s_waitcnt lgkmcnt(14)
	v_mfma_f32_32x32x16_bf16 v[0:15], v[204:207], v[68:71], v[0:15]
	ds_read_b64_tr_b16 v[204:205], v166 offset:18560
	ds_read_b64_tr_b16 v[206:207], v167 offset:19328
	s_waitcnt lgkmcnt(14)
	v_mfma_f32_32x32x16_bf16 v[32:47], v[224:227], v[76:79], v[32:47]
	ds_read_b128 v[224:227], v146
	s_waitcnt lgkmcnt(13)
	v_mfma_f32_32x32x16_bf16 v[16:31], v[228:231], v[76:79], v[16:31]
	ds_read_b128 v[228:231], v146 offset:12288
	s_waitcnt lgkmcnt(12)
	v_mfma_f32_32x32x16_bf16 v[32:47], v[232:235], v[72:75], v[32:47]
	ds_read_b128 v[232:235], v161
	s_waitcnt lgkmcnt(11)
	v_mfma_f32_32x32x16_bf16 v[16:31], v[236:239], v[72:75], v[16:31]
	ds_read_b128 v[236:239], v161 offset:12288
	s_waitcnt lgkmcnt(10)
	v_mfma_f32_32x32x16_bf16 v[32:47], v[240:243], v[64:67], v[32:47]
	ds_read_b128 v[240:243], v144
	s_waitcnt lgkmcnt(9)
	v_mfma_f32_32x32x16_bf16 v[16:31], v[244:247], v[64:67], v[16:31]
	ds_read_b128 v[244:247], v144 offset:12288
	s_waitcnt lgkmcnt(8)
	v_mfma_f32_32x32x16_bf16 v[32:47], v[252:255], v[68:71], v[32:47]
	ds_read_b128 v[252:255], v168
	s_waitcnt lgkmcnt(7)
	v_mfma_f32_32x32x16_bf16 v[16:31], v[204:207], v[68:71], v[16:31]
	ds_read_b128 v[204:207], v168 offset:12288
	s_waitcnt lgkmcnt(7)
	v_mfma_f32_32x32x16_bf16 v[80:95], v[224:227], v[112:115], 0
	ds_read_b128 v[224:227], v146 offset:128
	s_waitcnt lgkmcnt(7)
	v_mfma_f32_32x32x16_bf16 v[64:79], v[228:231], v[112:115], 0
	ds_read_b128 v[228:231], v146 offset:12416
	s_waitcnt lgkmcnt(7)
	v_mfma_f32_32x32x16_bf16 v[80:95], v[232:235], v[116:119], v[80:95]
	ds_read_b128 v[232:235], v161 offset:128
	s_waitcnt lgkmcnt(7)
	v_mfma_f32_32x32x16_bf16 v[64:79], v[236:239], v[116:119], v[64:79]
	ds_read_b128 v[236:239], v161 offset:12416
	s_waitcnt lgkmcnt(7)
	v_mfma_f32_32x32x16_bf16 v[80:95], v[240:243], v[120:123], v[80:95]
	ds_read_b128 v[240:243], v144 offset:128
	s_waitcnt lgkmcnt(7)
	v_mfma_f32_32x32x16_bf16 v[64:79], v[244:247], v[120:123], v[64:79]
	ds_read_b128 v[244:247], v144 offset:12416
	s_waitcnt lgkmcnt(7)
	v_mfma_f32_32x32x16_bf16 v[80:95], v[252:255], v[124:127], v[80:95]
	ds_read_b128 v[252:255], v168 offset:128
	s_waitcnt lgkmcnt(7)
	v_mfma_f32_32x32x16_bf16 v[64:79], v[204:207], v[124:127], v[64:79]
	ds_read_b128 v[204:207], v168 offset:12416
	s_waitcnt lgkmcnt(7)
	v_mfma_f32_32x32x16_bf16 v[80:95], v[224:227], v[96:99], v[80:95]
	ds_read_b128 v[224:227], v146 offset:256
	s_waitcnt lgkmcnt(7)
	v_mfma_f32_32x32x16_bf16 v[64:79], v[228:231], v[96:99], v[64:79]
	ds_read_b128 v[228:231], v146 offset:12544
	s_waitcnt lgkmcnt(7)
	v_mfma_f32_32x32x16_bf16 v[80:95], v[232:235], v[100:103], v[80:95]
	ds_read_b128 v[232:235], v161 offset:256
	s_waitcnt lgkmcnt(7)
	v_mfma_f32_32x32x16_bf16 v[64:79], v[236:239], v[100:103], v[64:79]
	ds_read_b128 v[236:239], v161 offset:12544
	s_waitcnt lgkmcnt(7)
	v_mfma_f32_32x32x16_bf16 v[80:95], v[240:243], v[104:107], v[80:95]
	ds_read_b128 v[240:243], v144 offset:256
	s_waitcnt lgkmcnt(7)
	v_mfma_f32_32x32x16_bf16 v[64:79], v[244:247], v[104:107], v[64:79]
	ds_read_b128 v[244:247], v144 offset:12544
	s_waitcnt lgkmcnt(7)
	v_mfma_f32_32x32x16_bf16 v[80:95], v[252:255], v[108:111], v[80:95]
	ds_read_b128 v[252:255], v168 offset:256
	s_waitcnt lgkmcnt(7)
	v_mfma_f32_32x32x16_bf16 v[64:79], v[204:207], v[108:111], v[64:79]
	ds_read_b128 v[204:207], v168 offset:12544
	s_waitcnt lgkmcnt(7)
	v_mfma_f32_32x32x16_bf16 v[80:95], v[224:227], v[128:131], v[80:95]
	s_waitcnt lgkmcnt(6)
	v_mfma_f32_32x32x16_bf16 v[64:79], v[228:231], v[128:131], v[64:79]
	s_waitcnt lgkmcnt(5)
	v_mfma_f32_32x32x16_bf16 v[80:95], v[232:235], v[132:135], v[80:95]
	s_waitcnt lgkmcnt(4)
	v_mfma_f32_32x32x16_bf16 v[64:79], v[236:239], v[132:135], v[64:79]
	s_waitcnt lgkmcnt(3)
	v_mfma_f32_32x32x16_bf16 v[80:95], v[240:243], v[136:139], v[80:95]
	s_waitcnt lgkmcnt(2)
	v_mfma_f32_32x32x16_bf16 v[64:79], v[244:247], v[136:139], v[64:79]
	s_waitcnt lgkmcnt(1)
	v_mfma_f32_32x32x16_bf16 v[80:95], v[252:255], v[140:143], v[80:95]
	s_waitcnt lgkmcnt(0)
	v_mfma_f32_32x32x16_bf16 v[64:79], v[204:207], v[140:143], v[64:79]
	s_waitcnt vmcnt(0)
	s_cmp_lt_u32 s88, 0x1000
	s_cbranch_scc1 .Lb3
	s_barrier
.Lb3:
	s_cmp_le_u32 s7, s44
	s_cbranch_scc1 .Lf_b
	v_add_u32_e32 v146, 59, v156
	v_cmp_le_i32_e64 s[16:17], 0, v146
	v_cmp_le_i32_e64 s[18:19], 32, v146
	v_cmp_le_i32_e64 vcc, 1, v146
	s_nop 4
	v_cndmask_b32_e64 v80, v199, v80, s[16:17]
	v_cmp_le_i32_e64 s[16:17], 33, v146
	v_cndmask_b32_e64 v64, v199, v64, s[18:19]
	v_cmp_le_i32_e64 s[18:19], 2, v146
	v_cndmask_b32_e64 v81, v199, v81, vcc
	v_cmp_le_i32_e64 vcc, 34, v146
	v_cndmask_b32_e64 v65, v199, v65, s[16:17]
	v_cmp_le_i32_e64 s[16:17], 3, v146
	v_cndmask_b32_e64 v82, v199, v82, s[18:19]
	v_cmp_le_i32_e64 s[18:19], 35, v146
	v_cndmask_b32_e64 v66, v199, v66, vcc
	v_cmp_le_i32_e64 vcc, 8, v146
	v_cndmask_b32_e64 v83, v199, v83, s[16:17]
	v_cmp_le_i32_e64 s[16:17], 40, v146
	v_cndmask_b32_e64 v67, v199, v67, s[18:19]
	v_cmp_le_i32_e64 s[18:19], 9, v146
	v_cndmask_b32_e64 v84, v199, v84, vcc
	v_cmp_le_i32_e64 vcc, 41, v146
	v_cndmask_b32_e64 v68, v199, v68, s[16:17]
	v_cmp_le_i32_e64 s[16:17], 10, v146
	v_cndmask_b32_e64 v85, v199, v85, s[18:19]
	v_cmp_le_i32_e64 s[18:19], 42, v146
	v_cndmask_b32_e64 v69, v199, v69, vcc
	v_cmp_le_i32_e64 vcc, 11, v146
	v_cndmask_b32_e64 v86, v199, v86, s[16:17]
	v_cmp_le_i32_e64 s[16:17], 43, v146
	v_cndmask_b32_e64 v70, v199, v70, s[18:19]
	v_cmp_le_i32_e64 s[18:19], 16, v146
	v_cndmask_b32_e64 v87, v199, v87, vcc
	v_cmp_le_i32_e64 vcc, 48, v146
	v_cndmask_b32_e64 v71, v199, v71, s[16:17]
	v_cmp_le_i32_e64 s[16:17], 17, v146
	v_cndmask_b32_e64 v88, v199, v88, s[18:19]
	v_cmp_le_i32_e64 s[18:19], 49, v146
	v_cndmask_b32_e64 v72, v199, v72, vcc
	v_cmp_le_i32_e64 vcc, 18, v146
	v_cndmask_b32_e64 v89, v199, v89, s[16:17]
	v_cmp_le_i32_e64 s[16:17], 50, v146
	v_cndmask_b32_e64 v73, v199, v73, s[18:19]
	v_cmp_le_i32_e64 s[18:19], 19, v146
	v_cndmask_b32_e64 v90, v199, v90, vcc
	v_cmp_le_i32_e64 vcc, 51, v146
	v_cndmask_b32_e64 v74, v199, v74, s[16:17]
	v_cmp_le_i32_e64 s[16:17], 24, v146
	v_cndmask_b32_e64 v91, v199, v91, s[18:19]
	v_cmp_le_i32_e64 s[18:19], 56, v146
	v_cndmask_b32_e64 v75, v199, v75, vcc
	v_cmp_le_i32_e64 vcc, 25, v146
	v_cndmask_b32_e64 v92, v199, v92, s[16:17]
	v_cmp_le_i32_e64 s[16:17], 57, v146
	v_cndmask_b32_e64 v76, v199, v76, s[18:19]
	v_cmp_le_i32_e64 s[18:19], 26, v146
	v_cndmask_b32_e64 v93, v199, v93, vcc
	v_cmp_le_i32_e64 vcc, 58, v146
	v_cndmask_b32_e64 v77, v199, v77, s[16:17]
	v_cmp_le_i32_e64 s[16:17], 27, v146
	v_cndmask_b32_e64 v94, v199, v94, s[18:19]
	v_cmp_le_i32_e64 s[18:19], 59, v146
	v_cndmask_b32_e64 v78, v199, v78, vcc
	v_cndmask_b32_e64 v95, v199, v95, s[16:17]
	v_cndmask_b32_e64 v79, v199, v79, s[18:19]

.Lno_bload2:
	s_add_i32 s98, s10, -1
	s_and_b32 s98, s98, 2
	s_mulk_i32 s98, 0x6000
	v_add_u32_e32 v209, s14, v151
	v_add_u32_e32 v210, s14, v152
	v_add_u32_e32 v213, s14, v153
	v_add_u32_e32 v214, s14, v154
	ds_read_b64_tr_b16 v[224:225], v209
	ds_read_b64_tr_b16 v[226:227], v210 offset:768
	ds_read_b64_tr_b16 v[228:229], v209 offset:128
	ds_read_b64_tr_b16 v[230:231], v210 offset:896
	ds_read_b64_tr_b16 v[232:233], v209 offset:6144
	ds_read_b64_tr_b16 v[234:235], v210 offset:6912
	ds_read_b64_tr_b16 v[236:237], v209 offset:6272
	ds_read_b64_tr_b16 v[238:239], v210 offset:7040
	ds_read_b64_tr_b16 v[240:241], v209 offset:12288
	ds_read_b64_tr_b16 v[242:243], v210 offset:13056
	ds_read_b64_tr_b16 v[244:245], v209 offset:12416
	ds_read_b64_tr_b16 v[246:247], v210 offset:13184
	v_exp_f32_e32 v170, v64
	v_exp_f32_e32 v171, v65
	v_exp_f32_e32 v176, v66
	v_exp_f32_e32 v177, v67
	v_exp_f32_e32 v178, v68
	v_exp_f32_e32 v179, v69
	v_exp_f32_e32 v161, v80
	v_exp_f32_e32 v185, v70
	v_exp_f32_e32 v162, v81
	v_exp_f32_e32 v187, v71
	v_exp_f32_e32 v163, v82
	v_exp_f32_e32 v203, v72
	v_exp_f32_e32 v164, v83
	v_exp_f32_e32 v204, v73
	v_exp_f32_e32 v165, v84
	v_exp_f32_e32 v205, v74
	v_exp_f32_e32 v166, v85
	v_exp_f32_e32 v206, v75
	v_exp_f32_e32 v167, v86
	v_exp_f32_e32 v207, v76
	v_exp_f32_e32 v168, v87
	v_exp_f32_e32 v208, v77
	v_exp_f32_e32 v88, v88
	v_exp_f32_e32 v89, v89
	v_exp_f32_e32 v90, v90
	v_exp_f32_e32 v91, v91
	v_cvt_pk_bf16_f32 v72, v161, v162
	v_cvt_pk_bf16_f32 v73, v165, v166
	v_cvt_pk_bf16_f32 v74, v163, v164
	v_cvt_pk_bf16_f32 v75, v167, v168
	v_exp_f32_e32 v92, v92
	v_exp_f32_e32 v93, v93
	v_exp_f32_e32 v94, v94
	v_exp_f32_e32 v95, v95
	v_exp_f32_e32 v211, v78
	v_mov_b32_e32 v80, v79
	v_cvt_pk_bf16_f32 v76, v88, v89
	v_cvt_pk_bf16_f32 v77, v92, v93
	v_cvt_pk_bf16_f32 v78, v90, v91
	v_cvt_pk_bf16_f32 v79, v94, v95
	v_cvt_pk_bf16_f32 v68, v170, v171
	v_cvt_pk_bf16_f32 v69, v178, v179
	v_cvt_pk_bf16_f32 v70, v176, v177
	v_cvt_pk_bf16_f32 v71, v185, v187
	v_exp_f32_e32 v212, v80
	v_cvt_pk_bf16_f32 v64, v203, v204
	v_cvt_pk_bf16_f32 v65, v207, v208
	v_cvt_pk_bf16_f32 v66, v205, v206
	v_cvt_pk_bf16_f32 v67, v211, v212
	v_add_f32_e32 v158, v158, v159
	s_addk_i32 s12, 0x1000
	s_add_i32 s11, s11, 4
	s_add_i32 s10, s10, 2
	s_addk_i32 s7, 0x80
	v_add_u32_e32 v155, 32, v155
	s_cmp_ge_u32 s13, s9
	v_add_u32_e32 v156, 0xffffff80, v156
	v_add_f32_e32 v84, 0, v161
	v_add_f32_e32 v84, v162, v84
	v_add_f32_e32 v84, v163, v84
	v_add_f32_e32 v84, v164, v84
	v_add_f32_e32 v144, v165, v84
	v_add_f32_e32 v80, v166, v144
	v_add_f32_e32 v80, v167, v80
	v_add_f32_e32 v80, v168, v80
	v_add_f32_e32 v80, v88, v80
	v_add_f32_e32 v88, v89, v80
	v_add_f32_e32 v84, v90, v88
	v_add_f32_e32 v84, v91, v84
	v_add_f32_e32 v84, v92, v84
	v_add_f32_e32 v84, v93, v84
	v_add_f32_e32 v88, v94, v84
	v_add_f32_e32 v80, v95, v88
	v_add_f32_e32 v80, v170, v80
	v_add_f32_e32 v80, v171, v80
	v_add_f32_e32 v80, v176, v80
	v_add_f32_e32 v88, v177, v80
	v_add_f32_e32 v248, v178, v88
	v_add_f32_e32 v249, v179, v248
	v_add_f32_e32 v252, v185, v249
	v_add_f32_e32 v253, v187, v252
	v_add_f32_e32 v84, v203, v253
	v_add_f32_e32 v254, v204, v84
	v_add_f32_e32 v255, v205, v254
	v_add_f32_e32 v248, v206, v255
	v_add_f32_e32 v249, v207, v248
	v_add_f32_e32 v80, v208, v249
	v_add_f32_e32 v252, v211, v80
	v_add_f32_e32 v253, v212, v252
	v_add_f32_e32 v158, v158, v253
	ds_read_b64_tr_b16 v[252:253], v209 offset:18432
	ds_read_b64_tr_b16 v[254:255], v210 offset:19200
	ds_read_b64_tr_b16 v[204:205], v209 offset:18560
	ds_read_b64_tr_b16 v[206:207], v210 offset:19328
	s_cmp_ge_u32 s88, 0x1000
	s_cbranch_scc1 .Lb4
	s_barrier
.Lb4:
	s_cmp_ge_u32 s13, s9
	v_add_u32_e32 v144, s98, v147
	v_add_u32_e32 v146, s98, v148
	v_add_u32_e32 v161, s98, v149
	v_add_u32_e32 v168, s98, v150
	s_waitcnt lgkmcnt(14)
	v_mfma_f32_32x32x16_bf16 v[48:63], v[224:227], v[72:75], v[48:63]
	ds_read_b64_tr_b16 v[224:225], v213
	ds_read_b64_tr_b16 v[226:227], v214 offset:768
	s_waitcnt lgkmcnt(14)
	v_mfma_f32_32x32x16_bf16 v[0:15], v[228:231], v[72:75], v[0:15]
	ds_read_b64_tr_b16 v[228:229], v213 offset:128
	ds_read_b64_tr_b16 v[230:231], v214 offset:896
	s_waitcnt lgkmcnt(14)
	v_mfma_f32_32x32x16_bf16 v[48:63], v[232:235], v[76:79], v[48:63]
	ds_read_b64_tr_b16 v[232:233], v213 offset:6144
	ds_read_b64_tr_b16 v[234:235], v214 offset:6912
	s_waitcnt lgkmcnt(14)
	v_mfma_f32_32x32x16_bf16 v[0:15], v[236:239], v[76:79], v[0:15]
	ds_read_b64_tr_b16 v[236:237], v213 offset:6272
	ds_read_b64_tr_b16 v[238:239], v214 offset:7040
	s_waitcnt lgkmcnt(14)
	v_mfma_f32_32x32x16_bf16 v[48:63], v[240:243], v[68:71], v[48:63]
	ds_read_b64_tr_b16 v[240:241], v213 offset:12288
	ds_read_b64_tr_b16 v[242:243], v214 offset:13056
	s_waitcnt lgkmcnt(14)
	v_mfma_f32_32x32x16_bf16 v[0:15], v[244:247], v[68:71], v[0:15]
	ds_read_b64_tr_b16 v[244:245], v213 offset:12416
	ds_read_b64_tr_b16 v[246:247], v214 offset:13184
	s_waitcnt lgkmcnt(14)
	v_mfma_f32_32x32x16_bf16 v[48:63], v[252:255], v[64:67], v[48:63]
	ds_read_b64_tr_b16 v[252:253], v213 offset:18432
	ds_read_b64_tr_b16 v[254:255], v214 offset:19200
	s_waitcnt lgkmcnt(14)
	v_mfma_f32_32x32x16_bf16 v[0:15], v[204:207], v[64:67], v[0:15]
	ds_read_b64_tr_b16 v[204:205], v213 offset:18560
	ds_read_b64_tr_b16 v[206:207], v214 offset:19328
	s_waitcnt lgkmcnt(14)
	v_mfma_f32_32x32x16_bf16 v[32:47], v[224:227], v[72:75], v[32:47]
	ds_read_b128 v[224:227], v144
	s_waitcnt lgkmcnt(13)
	v_mfma_f32_32x32x16_bf16 v[16:31], v[228:231], v[72:75], v[16:31]
	ds_read_b128 v[228:231], v144 offset:12288
	s_waitcnt lgkmcnt(12)
	v_mfma_f32_32x32x16_bf16 v[32:47], v[232:235], v[76:79], v[32:47]
	ds_read_b128 v[232:235], v146
	s_waitcnt lgkmcnt(11)
	v_mfma_f32_32x32x16_bf16 v[16:31], v[236:239], v[76:79], v[16:31]
	ds_read_b128 v[236:239], v146 offset:12288
	s_waitcnt lgkmcnt(10)
	v_mfma_f32_32x32x16_bf16 v[32:47], v[240:243], v[68:71], v[32:47]
	ds_read_b128 v[240:243], v161
	s_waitcnt lgkmcnt(9)
	v_mfma_f32_32x32x16_bf16 v[16:31], v[244:247], v[68:71], v[16:31]
	ds_read_b128 v[244:247], v161 offset:12288
	s_waitcnt lgkmcnt(8)
	v_mfma_f32_32x32x16_bf16 v[32:47], v[252:255], v[64:67], v[32:47]
	ds_read_b128 v[252:255], v168
	s_waitcnt lgkmcnt(7)
	v_mfma_f32_32x32x16_bf16 v[16:31], v[204:207], v[64:67], v[16:31]
	ds_read_b128 v[204:207], v168 offset:12288
	s_cbranch_scc1 .LBB0_1250
	s_add_i32 s13, s10, -1
	s_mov_b32 s14, s98
	s_waitcnt lgkmcnt(7)
	v_mfma_f32_32x32x16_bf16 v[80:95], v[224:227], v[112:115], 0
	ds_read_b128 v[224:227], v144 offset:128
	s_waitcnt lgkmcnt(7)
	v_mfma_f32_32x32x16_bf16 v[64:79], v[228:231], v[112:115], 0
	ds_read_b128 v[228:231], v144 offset:12416
	s_waitcnt lgkmcnt(7)
	v_mfma_f32_32x32x16_bf16 v[80:95], v[232:235], v[116:119], v[80:95]
	ds_read_b128 v[232:235], v146 offset:128
	s_waitcnt lgkmcnt(7)
	v_mfma_f32_32x32x16_bf16 v[64:79], v[236:239], v[116:119], v[64:79]
	ds_read_b128 v[236:239], v146 offset:12416
	s_waitcnt lgkmcnt(7)
	v_mfma_f32_32x32x16_bf16 v[80:95], v[240:243], v[120:123], v[80:95]
	ds_read_b128 v[240:243], v161 offset:128
	s_waitcnt lgkmcnt(7)
	v_mfma_f32_32x32x16_bf16 v[64:79], v[244:247], v[120:123], v[64:79]
	ds_read_b128 v[244:247], v161 offset:12416
	s_waitcnt lgkmcnt(7)
	v_mfma_f32_32x32x16_bf16 v[80:95], v[252:255], v[124:127], v[80:95]
	ds_read_b128 v[252:255], v168 offset:128
	s_waitcnt lgkmcnt(7)
	v_mfma_f32_32x32x16_bf16 v[64:79], v[204:207], v[124:127], v[64:79]
	ds_read_b128 v[204:207], v168 offset:12416
	s_waitcnt lgkmcnt(7)
	v_mfma_f32_32x32x16_bf16 v[80:95], v[224:227], v[96:99], v[80:95]
	ds_read_b128 v[224:227], v144 offset:256
	s_waitcnt lgkmcnt(7)
	v_mfma_f32_32x32x16_bf16 v[64:79], v[228:231], v[96:99], v[64:79]
	ds_read_b128 v[228:231], v144 offset:12544
	s_waitcnt lgkmcnt(7)
	v_mfma_f32_32x32x16_bf16 v[80:95], v[232:235], v[100:103], v[80:95]
	ds_read_b128 v[232:235], v146 offset:256
	s_waitcnt lgkmcnt(7)
	v_mfma_f32_32x32x16_bf16 v[64:79], v[236:239], v[100:103], v[64:79]
	ds_read_b128 v[236:239], v146 offset:12544
	s_waitcnt lgkmcnt(7)
	v_mfma_f32_32x32x16_bf16 v[80:95], v[240:243], v[104:107], v[80:95]
	ds_read_b128 v[240:243], v161 offset:256
	s_waitcnt lgkmcnt(7)
	v_mfma_f32_32x32x16_bf16 v[64:79], v[244:247], v[104:107], v[64:79]
	ds_read_b128 v[244:247], v161 offset:12544
	s_waitcnt lgkmcnt(7)
	v_mfma_f32_32x32x16_bf16 v[80:95], v[252:255], v[108:111], v[80:95]
	ds_read_b128 v[252:255], v168 offset:256
	s_waitcnt lgkmcnt(7)
	v_mfma_f32_32x32x16_bf16 v[64:79], v[204:207], v[108:111], v[64:79]
	ds_read_b128 v[204:207], v168 offset:12544
	s_waitcnt lgkmcnt(7)
	v_mfma_f32_32x32x16_bf16 v[80:95], v[224:227], v[128:131], v[80:95]
	s_waitcnt lgkmcnt(6)
	v_mfma_f32_32x32x16_bf16 v[64:79], v[228:231], v[128:131], v[64:79]
	s_waitcnt lgkmcnt(5)
	v_mfma_f32_32x32x16_bf16 v[80:95], v[232:235], v[132:135], v[80:95]
	s_waitcnt lgkmcnt(4)
	v_mfma_f32_32x32x16_bf16 v[64:79], v[236:239], v[132:135], v[64:79]
	s_waitcnt lgkmcnt(3)
	v_mfma_f32_32x32x16_bf16 v[80:95], v[240:243], v[136:139], v[80:95]
	s_waitcnt lgkmcnt(2)
	v_mfma_f32_32x32x16_bf16 v[64:79], v[244:247], v[136:139], v[64:79]
	s_waitcnt lgkmcnt(1)
	v_mfma_f32_32x32x16_bf16 v[80:95], v[252:255], v[140:143], v[80:95]
	s_waitcnt lgkmcnt(0)
	v_mfma_f32_32x32x16_bf16 v[64:79], v[204:207], v[140:143], v[64:79]
	s_waitcnt vmcnt(0)
	s_cmp_lt_u32 s88, 0x1000
	s_cbranch_scc1 .Lb1
	s_barrier
.Lb1:
	s_sub_i32 s15, s7, 64
	s_cmp_le_u32 s15, s44
	s_cbranch_scc1 .Lf_a
	v_add_u32_e32 v144, 123, v156
	v_cmp_le_i32_e64 s[16:17], 0, v144
	v_cmp_le_i32_e64 s[18:19], 32, v144
	v_cmp_le_i32_e64 vcc, 1, v144
	s_nop 4
	v_cndmask_b32_e64 v80, v199, v80, s[16:17]
	v_cmp_le_i32_e64 s[16:17], 33, v144
	v_cndmask_b32_e64 v64, v199, v64, s[18:19]
	v_cmp_le_i32_e64 s[18:19], 2, v144
	v_cndmask_b32_e64 v81, v199, v81, vcc
	v_cmp_le_i32_e64 vcc, 34, v144
	v_cndmask_b32_e64 v65, v199, v65, s[16:17]
	v_cmp_le_i32_e64 s[16:17], 3, v144
	v_cndmask_b32_e64 v82, v199, v82, s[18:19]
	v_cmp_le_i32_e64 s[18:19], 35, v144
	v_cndmask_b32_e64 v66, v199, v66, vcc
	v_cmp_le_i32_e64 vcc, 8, v144
	v_cndmask_b32_e64 v83, v199, v83, s[16:17]
	v_cmp_le_i32_e64 s[16:17], 40, v144
	v_cndmask_b32_e64 v67, v199, v67, s[18:19]
	v_cmp_le_i32_e64 s[18:19], 9, v144
	v_cndmask_b32_e64 v84, v199, v84, vcc
	v_cmp_le_i32_e64 vcc, 41, v144
	v_cndmask_b32_e64 v68, v199, v68, s[16:17]
	v_cmp_le_i32_e64 s[16:17], 10, v144
	v_cndmask_b32_e64 v85, v199, v85, s[18:19]
	v_cmp_le_i32_e64 s[18:19], 42, v144
	v_cndmask_b32_e64 v69, v199, v69, vcc
	v_cmp_le_i32_e64 vcc, 11, v144
	v_cndmask_b32_e64 v86, v199, v86, s[16:17]
	v_cmp_le_i32_e64 s[16:17], 43, v144
	v_cndmask_b32_e64 v70, v199, v70, s[18:19]
	v_cmp_le_i32_e64 s[18:19], 16, v144
	v_cndmask_b32_e64 v87, v199, v87, vcc
	v_cmp_le_i32_e64 vcc, 48, v144
	v_cndmask_b32_e64 v71, v199, v71, s[16:17]
	v_cmp_le_i32_e64 s[16:17], 17, v144
	v_cndmask_b32_e64 v88, v199, v88, s[18:19]
	v_cmp_le_i32_e64 s[18:19], 49, v144
	v_cndmask_b32_e64 v72, v199, v72, vcc
	v_cmp_le_i32_e64 vcc, 18, v144
	v_cndmask_b32_e64 v89, v199, v89, s[16:17]
	v_cmp_le_i32_e64 s[16:17], 50, v144
	v_cndmask_b32_e64 v73, v199, v73, s[18:19]
	v_cmp_le_i32_e64 s[18:19], 19, v144
	v_cndmask_b32_e64 v90, v199, v90, vcc
	v_cmp_le_i32_e64 vcc, 51, v144
	v_cndmask_b32_e64 v74, v199, v74, s[16:17]
	v_cmp_le_i32_e64 s[16:17], 24, v144
	v_cndmask_b32_e64 v91, v199, v91, s[18:19]
	v_cmp_le_i32_e64 s[18:19], 56, v144
	v_cndmask_b32_e64 v75, v199, v75, vcc
	v_cmp_le_i32_e64 vcc, 25, v144
	v_cndmask_b32_e64 v92, v199, v92, s[16:17]
	v_cmp_le_i32_e64 s[16:17], 57, v144
	v_cndmask_b32_e64 v76, v199, v76, s[18:19]
	v_cmp_le_i32_e64 s[18:19], 26, v144
	v_cndmask_b32_e64 v93, v199, v93, vcc
	v_cmp_le_i32_e64 vcc, 58, v144
	v_cndmask_b32_e64 v77, v199, v77, s[16:17]
	v_cmp_le_i32_e64 s[16:17], 27, v144
	v_cndmask_b32_e64 v94, v199, v94, s[18:19]
	v_cmp_le_i32_e64 s[18:19], 59, v144
	v_cndmask_b32_e64 v78, v199, v78, vcc
	v_cndmask_b32_e64 v95, v199, v95, s[16:17]
	v_cndmask_b32_e64 v79, v199, v79, s[18:19]
	s_branch .Lf_a
.LBB0_1250:
	s_waitcnt vmcnt(0) lgkmcnt(0)
.Lnostag_out:
	s_cmp_eq_u32 s101, 0
	s_cbranch_scc1 .Lg_done
	v_mov_b32_e32 v160, v158
	s_nop 1
	v_permlane32_swap_b32_e32 v158, v160
	v_add_f32_e32 v158, v158, v160
	v_cmp_gt_f32_e32 vcc, 0x7149f2ca, v158
	s_mov_b64 s[16:17], vcc
	v_cmp_lt_f32_e32 vcc, 0x0da24260, v158
	s_and_b64 vcc, vcc, s[16:17]
	v_mov_b32_e32 v159, 0x20180
	s_cmp_eq_u64 vcc, exec
	s_cbranch_scc1 .Lg_vote
	v_mov_b32_e32 v160, 1
	ds_write_b32 v159, v160
